# v91 plus three small edits together: exact counted waits in the MoE gate/up epilogue, router bias words preloaded, leader invalidate issued before the top-level arrival
# speedup vs baseline: 1.0021x; 1.0021x over previous
; __device__ __forceinline__ unsigned cvt_pk_bf16(float lo, float hi) { unsigned r; asm volatile("v_cvt_pk_bf16_f32 %0, %1, %2" : "=v"(r) : "v"(lo), "v"(hi)); return r; }
; __device__ __forceinline__ void st_wt16(void* p, u32x4 v) { asm volatile("global_store_dwordx4 %0, %1, off sc1\n\ts_nop 1" :: "v"(p), "v"(v) : "memory"); }
;     __device__ __forceinline__ void operator()(const f32x4 (&acc)[2][2][4][2], const Unit& u, int wr, int wc, int fr, int fq) const {
;         const int f0 = u.pn * 128 + wc * 32 + 8 * fq;
;         int slots[8]; float scv[8], gwv[8];
; #pragma unroll
;         for (int j = 0; j < 8; ++j) { const int r = (j >> 2) * HALF + wr * 64 + (j & 3) * 16 + fr; slots[j] = list[u.e * LCAP + u.pm * BM + (r < u.rows ? r : u.rows - 1)]; }
; #pragma unroll
;         for (int j = 0; j < 8; ++j) { scv[j] = rsc ? rsc[slots[j]] * cs : cs; gwv[j] = gatew[slots[j]]; }
; #pragma unroll
;         for (int ai = 0; ai < 2; ++ai)
; #pragma unroll
;             for (int m = 0; m < 4; ++m) {
;                 const int r = ai * HALF + wr * 64 + m * 16 + fr; const bool valid = r < u.rows;
;                 const int slot = slots[ai * 4 + m];
;                 const float sc = scv[ai * 4 + m], gw = gwv[ai * 4 + m]; float o[8];
; #pragma unroll
;                 for (int n = 0; n < 2; ++n) { const f32x4 g = acc[ai][0][m][n] * sc, up = acc[ai][1][m][n] * sc;
; #pragma unroll
;                     for (int j = 0; j < 4; ++j) o[4 * n + j] = g[j] * __builtin_amdgcn_rcpf(1.0f + __expf(-g[j])) * up[j] * gw; }
;                 u32x4 w; w.x = cvt_pk_bf16(o[0], o[1]); w.y = cvt_pk_bf16(o[2], o[3]); w.z = cvt_pk_bf16(o[4], o[5]); w.w = cvt_pk_bf16(o[6], o[7]);
;                 if (valid) st_wt16(hid + (size_t)slot * 512 + f0, w);
;             }
.LBB0_1605:
	v_mbcnt_lo_u32_b32 v64, -1, 0
	v_mbcnt_hi_u32_b32 v64, -1, v64
	s_lshl_b32 s0, s6, 14
	v_add_u32_e32 v130, s93, v64
	s_lshl_b32 s1, s33, 8
	v_and_b32_e32 v64, 15, v130
	s_add_i32 s0, s0, s1
	s_add_i32 s1, s40, -1
	v_or_b32_e32 v156, s49, v64
	v_bfe_u32 v155, v130, 4, 2
	v_min_i32_e32 v130, s1, v156
	v_add_u32_e32 v130, s0, v130
	v_ashrrev_i32_e32 v131, 31, v130
	v_lshl_add_u64 v[130:131], v[130:131], 2, s[12:13]
	global_load_dword v152, v[130:131], off
	v_or_b32_e32 v165, 16, v156
	v_min_i32_e32 v130, s1, v165
	v_add_u32_e32 v130, s0, v130
	v_ashrrev_i32_e32 v131, 31, v130
	v_lshl_add_u64 v[130:131], v[130:131], 2, s[12:13]
	v_or_b32_e32 v163, 32, v156
	global_load_dword v144, v[130:131], off
	v_min_i32_e32 v130, s1, v163
	v_add_u32_e32 v130, s0, v130
	v_ashrrev_i32_e32 v131, 31, v130
	v_lshl_add_u64 v[130:131], v[130:131], 2, s[12:13]
	v_or_b32_e32 v161, 48, v156
	global_load_dword v142, v[130:131], off
	v_min_i32_e32 v130, s1, v161
	v_add_u32_e32 v130, s0, v130
	v_ashrrev_i32_e32 v131, 31, v130
	v_lshl_add_u64 v[130:131], v[130:131], 2, s[12:13]
	v_or_b32_e32 v132, s56, v64
	global_load_dword v140, v[130:131], off
	v_min_i32_e32 v130, s1, v132
	v_add_u32_e32 v130, s0, v130
	v_ashrrev_i32_e32 v131, 31, v130
	v_lshl_add_u64 v[130:131], v[130:131], 2, s[12:13]
	global_load_dword v138, v[130:131], off
	v_or_b32_e32 v130, 16, v132
	v_min_i32_e32 v130, s1, v130
	v_add_u32_e32 v130, s0, v130
	v_ashrrev_i32_e32 v131, 31, v130
	v_lshl_add_u64 v[130:131], v[130:131], 2, s[12:13]
	global_load_dword v136, v[130:131], off
	v_or_b32_e32 v130, 32, v132
	v_min_i32_e32 v130, s1, v130
	v_add_u32_e32 v130, s0, v130
	v_ashrrev_i32_e32 v131, 31, v130
	v_lshl_add_u64 v[130:131], v[130:131], 2, s[12:13]
	global_load_dword v134, v[130:131], off
	v_or_b32_e32 v130, 48, v132
	v_min_i32_e32 v130, s1, v130
	v_add_u32_e32 v130, s0, v130
	v_ashrrev_i32_e32 v131, 31, v130
	v_lshl_add_u64 v[130:131], v[130:131], 2, s[12:13]
	global_load_dword v130, v[130:131], off
	v_mul_f32_e32 v126, 0x3c800000, v126
	v_mul_f32_e32 v147, 0xbfb8aa3b, v126
	v_exp_f32_e32 v147, v147
	v_mul_f32_e32 v122, 0x3c800000, v122
	v_mul_f32_e32 v123, 0x3c800000, v123
	v_mul_f32_e32 v124, 0x3c800000, v124
	v_add_f32_e32 v147, 1.0, v147
	v_rcp_f32_e32 v147, v147
	v_mul_f32_e32 v125, 0x3c800000, v125
	v_mul_f32_e32 v118, 0x3c800000, v118
	v_mul_f32_e32 v114, 0x3c800000, v114
	v_mul_f32_e32 v126, v126, v147
	v_mul_f32_e32 v122, v126, v122
	v_mul_f32_e32 v126, 0x3c800000, v127
	v_mul_f32_e32 v127, 0xbfb8aa3b, v126
	v_exp_f32_e32 v127, v127
	v_mul_f32_e32 v115, 0x3c800000, v115
	s_lshl_b32 s0, s28, 7
	v_cmp_gt_i32_e32 vcc, s40, v156
	v_add_f32_e32 v127, 1.0, v127
	v_rcp_f32_e32 v127, v127
	s_waitcnt vmcnt(0)
	v_ashrrev_i32_e32 v153, 31, v152
	v_lshl_add_u64 v[132:133], v[152:153], 2, s[16:17]
	global_load_dword v146, v[132:133], off
	v_mul_f32_e32 v126, v126, v127
	v_mul_f32_e32 v123, v126, v123
	v_mul_f32_e32 v126, 0x3c800000, v128
	v_mul_f32_e32 v127, 0xbfb8aa3b, v126
	v_ashrrev_i32_e32 v145, 31, v144
	v_lshl_add_u64 v[132:133], v[144:145], 2, s[16:17]
	global_load_dword v166, v[132:133], off
	v_exp_f32_e32 v127, v127
	v_ashrrev_i32_e32 v143, 31, v142
	v_lshl_add_u64 v[132:133], v[142:143], 2, s[16:17]
	global_load_dword v164, v[132:133], off
	v_add_f32_e32 v127, 1.0, v127
	v_rcp_f32_e32 v127, v127
	v_ashrrev_i32_e32 v141, 31, v140
	v_lshl_add_u64 v[132:133], v[140:141], 2, s[16:17]
	global_load_dword v162, v[132:133], off
	v_mul_f32_e32 v126, v126, v127
	v_mul_f32_e32 v124, v126, v124
	v_ashrrev_i32_e32 v139, 31, v138
	v_lshl_add_u64 v[132:133], v[138:139], 2, s[16:17]
	global_load_dword v160, v[132:133], off
	v_mul_f32_e32 v126, 0x3c800000, v129
	v_mul_f32_e32 v127, 0xbfb8aa3b, v126
	v_exp_f32_e32 v127, v127
	v_ashrrev_i32_e32 v137, 31, v136
	v_lshl_add_u64 v[132:133], v[136:137], 2, s[16:17]
	global_load_dword v159, v[132:133], off
	v_add_f32_e32 v127, 1.0, v127
	v_rcp_f32_e32 v127, v127
	v_ashrrev_i32_e32 v135, 31, v134
	v_lshl_add_u64 v[132:133], v[134:135], 2, s[16:17]
	global_load_dword v158, v[132:133], off
	v_mul_f32_e32 v126, v126, v127
	v_mul_f32_e32 v125, v126, v125
	v_mul_f32_e32 v126, 0xbfb8aa3b, v118
	v_ashrrev_i32_e32 v131, 31, v130
	v_lshl_add_u64 v[132:133], v[130:131], 2, s[16:17]
	global_load_dword v157, v[132:133], off
	v_exp_f32_e32 v126, v126
	v_lshl_or_b32 v132, v155, 3, s0
	v_or_b32_e32 v132, s50, v132
	v_ashrrev_i32_e32 v133, 31, v132
	v_add_f32_e32 v126, 1.0, v126
	v_rcp_f32_e32 v126, v126
	s_waitcnt vmcnt(7)
	v_mul_f32_e32 v122, v122, v146
	v_mul_f32_e32 v118, v118, v126
	v_mul_f32_e32 v114, v118, v114
	v_mul_f32_e32 v118, v114, v146
	v_mul_f32_e32 v114, 0x3c800000, v119
	v_mul_f32_e32 v119, 0xbfb8aa3b, v114
	v_exp_f32_e32 v119, v119
	v_mul_f32_e32 v123, v123, v146
	v_mul_f32_e32 v124, v124, v146
	v_mul_f32_e32 v125, v125, v146
	v_add_f32_e32 v119, 1.0, v119
	v_rcp_f32_e32 v119, v119
	s_nop 0
	v_mul_f32_e32 v114, v114, v119
	v_mul_f32_e32 v114, v114, v115
	v_mul_f32_e32 v119, v114, v146
	v_mul_f32_e32 v114, 0x3c800000, v120
	v_mul_f32_e32 v115, 0xbfb8aa3b, v114
	v_exp_f32_e32 v115, v115
	s_nop 0
	v_add_f32_e32 v115, 1.0, v115
	v_rcp_f32_e32 v115, v115
	s_nop 0
	v_mul_f32_e32 v114, v114, v115
	v_mul_f32_e32 v115, 0x3c800000, v116
	v_mul_f32_e32 v114, v114, v115
	v_mul_f32_e32 v120, v114, v146
	v_mul_f32_e32 v114, 0x3c800000, v121
	v_mul_f32_e32 v115, 0xbfb8aa3b, v114
	v_exp_f32_e32 v115, v115
	s_nop 0
	v_add_f32_e32 v115, 1.0, v115
	v_rcp_f32_e32 v115, v115
	s_nop 0
	v_mul_f32_e32 v114, v114, v115
	v_mul_f32_e32 v115, 0x3c800000, v117
	v_mul_f32_e32 v114, v114, v115
	v_mul_f32_e32 v117, v114, v146
	v_cvt_pk_bf16_f32 v114, v122, v123
	v_cvt_pk_bf16_f32 v115, v124, v125
	v_cvt_pk_bf16_f32 v116, v118, v119
	v_cvt_pk_bf16_f32 v117, v120, v117
	s_and_saveexec_b64 s[0:1], vcc
	v_lshlrev_b64 v[118:119], 10, v[152:153]
	v_lshl_add_u64 v[118:119], s[10:11], 0, v[118:119]
	v_lshl_add_u64 v[118:119], v[132:133], 1, v[118:119]
	global_store_dwordx4 v[118:119], v[114:117], off sc1
	s_nop 1
; __device__ __forceinline__ unsigned cvt_pk_bf16(float lo, float hi) { unsigned r; asm volatile("v_cvt_pk_bf16_f32 %0, %1, %2" : "=v"(r) : "v"(lo), "v"(hi)); return r; }
; __device__ __forceinline__ void st_wt16(void* p, u32x4 v) { asm volatile("global_store_dwordx4 %0, %1, off sc1\n\ts_nop 1" :: "v"(p), "v"(v) : "memory"); }
;     __device__ __forceinline__ void operator()(const f32x4 (&acc)[2][2][4][2], const Unit& u, int wr, int wc, int fr, int fq) const {
;     ...
;         for (int ai = 0; ai < 2; ++ai)
; #pragma unroll
;             for (int m = 0; m < 4; ++m) {
;                 const int r = ai * HALF + wr * 64 + m * 16 + fr; const bool valid = r < u.rows;
;                 const int slot = slots[ai * 4 + m];
;                 const float sc = scv[ai * 4 + m], gw = gwv[ai * 4 + m]; float o[8];
; #pragma unroll
;                 for (int n = 0; n < 2; ++n) { const f32x4 g = acc[ai][0][m][n] * sc, up = acc[ai][1][m][n] * sc;
; #pragma unroll
;                     for (int j = 0; j < 4; ++j) o[4 * n + j] = g[j] * __builtin_amdgcn_rcpf(1.0f + __expf(-g[j])) * up[j] * gw; }
;                 u32x4 w; w.x = cvt_pk_bf16(o[0], o[1]); w.y = cvt_pk_bf16(o[2], o[3]); w.z = cvt_pk_bf16(o[4], o[5]); w.w = cvt_pk_bf16(o[6], o[7]);
;                 if (valid) st_wt16(hid + (size_t)slot * 512 + f0, w);
;             }
.LBB0_1607:
	s_or_b64 exec, exec, s[0:1]
	v_mul_f32_e32 v110, 0x3c800000, v110
	v_mul_f32_e32 v114, 0xbfb8aa3b, v110
	v_exp_f32_e32 v114, v114
	v_mul_f32_e32 v106, 0x3c800000, v106
	v_mul_f32_e32 v107, 0x3c800000, v107
	v_mul_f32_e32 v108, 0x3c800000, v108
	v_add_f32_e32 v114, 1.0, v114
	v_rcp_f32_e32 v114, v114
	v_mul_f32_e32 v109, 0x3c800000, v109
	v_mul_f32_e32 v102, 0x3c800000, v102
	v_mul_f32_e32 v98, 0x3c800000, v98
	v_mul_f32_e32 v110, v110, v114
	v_mul_f32_e32 v106, v110, v106
	v_mul_f32_e32 v110, 0x3c800000, v111
	v_mul_f32_e32 v111, 0xbfb8aa3b, v110
	v_exp_f32_e32 v111, v111
	v_mul_f32_e32 v99, 0x3c800000, v99
	v_cmp_gt_i32_e32 vcc, s40, v165
	s_waitcnt vmcnt(7)
	v_mul_f32_e32 v106, v106, v166
	v_add_f32_e32 v111, 1.0, v111
	v_rcp_f32_e32 v111, v111
	s_nop 0
	v_mul_f32_e32 v110, v110, v111
	v_mul_f32_e32 v107, v110, v107
	v_mul_f32_e32 v110, 0x3c800000, v112
	v_mul_f32_e32 v111, 0xbfb8aa3b, v110
	v_exp_f32_e32 v111, v111
	v_mul_f32_e32 v107, v107, v166
	v_add_f32_e32 v111, 1.0, v111
	v_rcp_f32_e32 v111, v111
	s_nop 0
	v_mul_f32_e32 v110, v110, v111
	v_mul_f32_e32 v108, v110, v108
	v_mul_f32_e32 v110, 0x3c800000, v113
	v_mul_f32_e32 v111, 0xbfb8aa3b, v110
	v_exp_f32_e32 v111, v111
	v_mul_f32_e32 v108, v108, v166
	v_add_f32_e32 v111, 1.0, v111
	v_rcp_f32_e32 v111, v111
	s_nop 0
	v_mul_f32_e32 v110, v110, v111
	v_mul_f32_e32 v109, v110, v109
	v_mul_f32_e32 v110, 0xbfb8aa3b, v102
	v_exp_f32_e32 v110, v110
	v_mul_f32_e32 v109, v109, v166
	v_add_f32_e32 v110, 1.0, v110
	v_rcp_f32_e32 v110, v110
	s_nop 0
	v_mul_f32_e32 v102, v102, v110
	v_mul_f32_e32 v98, v102, v98
	v_mul_f32_e32 v102, v98, v166
	v_mul_f32_e32 v98, 0x3c800000, v103
	v_mul_f32_e32 v103, 0xbfb8aa3b, v98
	v_exp_f32_e32 v103, v103
	s_nop 0
	v_add_f32_e32 v103, 1.0, v103
	v_rcp_f32_e32 v103, v103
	s_nop 0
	v_mul_f32_e32 v98, v98, v103
	v_mul_f32_e32 v98, v98, v99
	v_mul_f32_e32 v103, v98, v166
	v_mul_f32_e32 v98, 0x3c800000, v104
	v_mul_f32_e32 v99, 0xbfb8aa3b, v98
	v_exp_f32_e32 v99, v99
	s_nop 0
	v_add_f32_e32 v99, 1.0, v99
	v_rcp_f32_e32 v99, v99
	s_nop 0
	v_mul_f32_e32 v98, v98, v99
	v_mul_f32_e32 v99, 0x3c800000, v100
	v_mul_f32_e32 v98, v98, v99
	v_mul_f32_e32 v104, v98, v166
	v_mul_f32_e32 v98, 0x3c800000, v105
	v_mul_f32_e32 v99, 0xbfb8aa3b, v98
	v_exp_f32_e32 v99, v99
	s_nop 0
	v_add_f32_e32 v99, 1.0, v99
	v_rcp_f32_e32 v99, v99
	s_nop 0
	v_mul_f32_e32 v98, v98, v99
	v_mul_f32_e32 v99, 0x3c800000, v101
	v_mul_f32_e32 v98, v98, v99
	v_mul_f32_e32 v101, v98, v166
	v_cvt_pk_bf16_f32 v98, v106, v107
	v_cvt_pk_bf16_f32 v99, v108, v109
	v_cvt_pk_bf16_f32 v100, v102, v103
	v_cvt_pk_bf16_f32 v101, v104, v101
	s_and_saveexec_b64 s[0:1], vcc
	v_lshlrev_b64 v[102:103], 10, v[144:145]
	v_lshl_add_u64 v[102:103], s[10:11], 0, v[102:103]
	v_lshl_add_u64 v[102:103], v[132:133], 1, v[102:103]
	global_store_dwordx4 v[102:103], v[98:101], off sc1
	s_nop 1
.LBB0_1609:
	s_or_b64 exec, exec, s[0:1]
	v_mul_f32_e32 v94, 0x3c800000, v94
	v_mul_f32_e32 v98, 0xbfb8aa3b, v94
	v_exp_f32_e32 v98, v98
	v_mul_f32_e32 v90, 0x3c800000, v90
	v_mul_f32_e32 v91, 0x3c800000, v91
	v_mul_f32_e32 v92, 0x3c800000, v92
	v_add_f32_e32 v98, 1.0, v98
	v_rcp_f32_e32 v98, v98
	v_mul_f32_e32 v93, 0x3c800000, v93
	v_mul_f32_e32 v86, 0x3c800000, v86
	v_mul_f32_e32 v82, 0x3c800000, v82
	v_mul_f32_e32 v94, v94, v98
	v_mul_f32_e32 v90, v94, v90
	v_mul_f32_e32 v94, 0x3c800000, v95
	v_mul_f32_e32 v95, 0xbfb8aa3b, v94
	v_exp_f32_e32 v95, v95
	v_mul_f32_e32 v83, 0x3c800000, v83
	s_waitcnt vmcnt(7)
	v_mul_f32_e32 v90, v90, v164
	v_cmp_gt_i32_e32 vcc, s40, v163
	v_add_f32_e32 v95, 1.0, v95
	v_rcp_f32_e32 v95, v95
	s_nop 0
	v_mul_f32_e32 v94, v94, v95
	v_mul_f32_e32 v91, v94, v91
	v_mul_f32_e32 v94, 0x3c800000, v96
	v_mul_f32_e32 v95, 0xbfb8aa3b, v94
	v_exp_f32_e32 v95, v95
	v_mul_f32_e32 v91, v91, v164
	v_add_f32_e32 v95, 1.0, v95
	v_rcp_f32_e32 v95, v95
	s_nop 0
	v_mul_f32_e32 v94, v94, v95
	v_mul_f32_e32 v92, v94, v92
	v_mul_f32_e32 v94, 0x3c800000, v97
	v_mul_f32_e32 v95, 0xbfb8aa3b, v94
	v_exp_f32_e32 v95, v95
	v_mul_f32_e32 v92, v92, v164
	v_add_f32_e32 v95, 1.0, v95
	v_rcp_f32_e32 v95, v95
	s_nop 0
	v_mul_f32_e32 v94, v94, v95
	v_mul_f32_e32 v93, v94, v93
	v_mul_f32_e32 v94, 0xbfb8aa3b, v86
	v_exp_f32_e32 v94, v94
	v_mul_f32_e32 v93, v93, v164
	v_add_f32_e32 v94, 1.0, v94
	v_rcp_f32_e32 v94, v94
	s_nop 0
	v_mul_f32_e32 v86, v86, v94
	v_mul_f32_e32 v82, v86, v82
	v_mul_f32_e32 v86, v82, v164
	v_mul_f32_e32 v82, 0x3c800000, v87
	v_mul_f32_e32 v87, 0xbfb8aa3b, v82
	v_exp_f32_e32 v87, v87
	s_nop 0
	v_add_f32_e32 v87, 1.0, v87
	v_rcp_f32_e32 v87, v87
	s_nop 0
	v_mul_f32_e32 v82, v82, v87
	v_mul_f32_e32 v82, v82, v83
	v_mul_f32_e32 v87, v82, v164
	v_mul_f32_e32 v82, 0x3c800000, v88
	v_mul_f32_e32 v83, 0xbfb8aa3b, v82
	v_exp_f32_e32 v83, v83
	s_nop 0
	v_add_f32_e32 v83, 1.0, v83
	v_rcp_f32_e32 v83, v83
	s_nop 0
	v_mul_f32_e32 v82, v82, v83
	v_mul_f32_e32 v83, 0x3c800000, v84
	v_mul_f32_e32 v82, v82, v83
	v_mul_f32_e32 v88, v82, v164
	v_mul_f32_e32 v82, 0x3c800000, v89
	v_mul_f32_e32 v83, 0xbfb8aa3b, v82
	v_exp_f32_e32 v83, v83
	s_nop 0
	v_add_f32_e32 v83, 1.0, v83
	v_rcp_f32_e32 v83, v83
	s_nop 0
	v_mul_f32_e32 v82, v82, v83
	v_mul_f32_e32 v83, 0x3c800000, v85
	v_mul_f32_e32 v82, v82, v83
	v_mul_f32_e32 v85, v82, v164
	v_cvt_pk_bf16_f32 v82, v90, v91
	v_cvt_pk_bf16_f32 v83, v92, v93
	v_cvt_pk_bf16_f32 v84, v86, v87
	v_cvt_pk_bf16_f32 v85, v88, v85
	s_mov_b64 s[0:1], exec
	s_and_b64 s[30:31], s[0:1], vcc
	v_mov_b32_e32 v218, 0x358637bd
	v_mov_b32_e32 v219, 0x43e00000
	v_mov_b32_e32 v226, 0xff800000
	v_mov_b64_e32 v[228:229], 0x1e8481
	s_mov_b64 exec, s[30:31]
	v_lshlrev_b64 v[86:87], 10, v[142:143]
	v_lshl_add_u64 v[86:87], s[10:11], 0, v[86:87]
	v_lshl_add_u64 v[86:87], v[132:133], 1, v[86:87]
	global_store_dwordx4 v[86:87], v[82:85], off sc1
	s_nop 1
; __device__ __forceinline__ unsigned cvt_pk_bf16(float lo, float hi) { unsigned r; asm volatile("v_cvt_pk_bf16_f32 %0, %1, %2" : "=v"(r) : "v"(lo), "v"(hi)); return r; }
; __device__ __forceinline__ void st_wt16(void* p, u32x4 v) { asm volatile("global_store_dwordx4 %0, %1, off sc1\n\ts_nop 1" :: "v"(p), "v"(v) : "memory"); }
;     __device__ __forceinline__ void operator()(const f32x4 (&acc)[2][2][4][2], const Unit& u, int wr, int wc, int fr, int fq) const {
;     ...
;         for (int ai = 0; ai < 2; ++ai)
; #pragma unroll
;             for (int m = 0; m < 4; ++m) {
;                 const int r = ai * HALF + wr * 64 + m * 16 + fr; const bool valid = r < u.rows;
;                 const int slot = slots[ai * 4 + m];
;                 const float sc = scv[ai * 4 + m], gw = gwv[ai * 4 + m]; float o[8];
; #pragma unroll
;                 for (int n = 0; n < 2; ++n) { const f32x4 g = acc[ai][0][m][n] * sc, up = acc[ai][1][m][n] * sc;
; #pragma unroll
;                     for (int j = 0; j < 4; ++j) o[4 * n + j] = g[j] * __builtin_amdgcn_rcpf(1.0f + __expf(-g[j])) * up[j] * gw; }
;                 u32x4 w; w.x = cvt_pk_bf16(o[0], o[1]); w.y = cvt_pk_bf16(o[2], o[3]); w.z = cvt_pk_bf16(o[4], o[5]); w.w = cvt_pk_bf16(o[6], o[7]);
;                 if (valid) st_wt16(hid + (size_t)slot * 512 + f0, w);
;             }
.LBB0_1611:
	s_or_b64 exec, exec, s[0:1]
	v_mul_f32_e32 v78, 0x3c800000, v78
	v_mul_f32_e32 v82, 0xbfb8aa3b, v78
	v_exp_f32_e32 v82, v82
	v_mul_f32_e32 v74, 0x3c800000, v74
	v_mul_f32_e32 v75, 0x3c800000, v75
	v_mul_f32_e32 v76, 0x3c800000, v76
	v_add_f32_e32 v82, 1.0, v82
	v_rcp_f32_e32 v82, v82
	v_mul_f32_e32 v77, 0x3c800000, v77
	v_mul_f32_e32 v70, 0x3c800000, v70
	v_mul_f32_e32 v66, 0x3c800000, v12
	v_mul_f32_e32 v78, v78, v82
	v_mul_f32_e32 v74, v78, v74
	v_mul_f32_e32 v78, 0x3c800000, v79
	v_mul_f32_e32 v79, 0xbfb8aa3b, v78
	v_exp_f32_e32 v79, v79
	v_mul_f32_e32 v67, 0x3c800000, v13
	v_cmp_gt_i32_e32 vcc, s40, v161
	s_waitcnt vmcnt(7)
	v_mul_f32_e32 v74, v74, v162
	v_add_f32_e32 v79, 1.0, v79
	v_rcp_f32_e32 v79, v79
	s_nop 0
	v_mul_f32_e32 v78, v78, v79
	v_mul_f32_e32 v75, v78, v75
	v_mul_f32_e32 v78, 0x3c800000, v80
	v_mul_f32_e32 v79, 0xbfb8aa3b, v78
	v_exp_f32_e32 v79, v79
	v_mul_f32_e32 v75, v75, v162
	v_add_f32_e32 v79, 1.0, v79
	v_rcp_f32_e32 v79, v79
	s_nop 0
	v_mul_f32_e32 v78, v78, v79
	v_mul_f32_e32 v76, v78, v76
	v_mul_f32_e32 v78, 0x3c800000, v81
	v_mul_f32_e32 v79, 0xbfb8aa3b, v78
	v_exp_f32_e32 v79, v79
	v_mul_f32_e32 v76, v76, v162
	v_add_f32_e32 v79, 1.0, v79
	v_rcp_f32_e32 v79, v79
	s_nop 0
	v_mul_f32_e32 v78, v78, v79
	v_mul_f32_e32 v77, v78, v77
	v_mul_f32_e32 v78, 0xbfb8aa3b, v70
	v_exp_f32_e32 v78, v78
	v_mul_f32_e32 v77, v77, v162
	v_add_f32_e32 v78, 1.0, v78
	v_rcp_f32_e32 v78, v78
	s_nop 0
	v_mul_f32_e32 v70, v70, v78
	v_mul_f32_e32 v66, v70, v66
	v_mul_f32_e32 v70, v66, v162
	v_mul_f32_e32 v66, 0x3c800000, v71
	v_mul_f32_e32 v71, 0xbfb8aa3b, v66
	v_exp_f32_e32 v71, v71
	s_nop 0
	v_add_f32_e32 v71, 1.0, v71
	v_rcp_f32_e32 v71, v71
	s_nop 0
	v_mul_f32_e32 v66, v66, v71
	v_mul_f32_e32 v66, v66, v67
	v_mul_f32_e32 v71, v66, v162
	v_mul_f32_e32 v66, 0x3c800000, v72
	v_mul_f32_e32 v67, 0xbfb8aa3b, v66
	v_exp_f32_e32 v67, v67
	s_nop 0
	v_add_f32_e32 v67, 1.0, v67
	v_rcp_f32_e32 v67, v67
	s_nop 0
	v_mul_f32_e32 v66, v66, v67
	v_mul_f32_e32 v67, 0x3c800000, v14
	v_mul_f32_e32 v66, v66, v67
	v_mul_f32_e32 v72, v66, v162
	v_mul_f32_e32 v66, 0x3c800000, v73
	v_mul_f32_e32 v67, 0xbfb8aa3b, v66
	v_exp_f32_e32 v67, v67
	s_nop 0
	v_add_f32_e32 v67, 1.0, v67
	v_rcp_f32_e32 v67, v67
	s_nop 0
	v_mul_f32_e32 v66, v66, v67
	v_mul_f32_e32 v67, 0x3c800000, v15
	v_mul_f32_e32 v66, v66, v67
	v_mul_f32_e32 v69, v66, v162
	v_cvt_pk_bf16_f32 v66, v74, v75
	v_cvt_pk_bf16_f32 v67, v76, v77
	v_cvt_pk_bf16_f32 v68, v70, v71
	v_cvt_pk_bf16_f32 v69, v72, v69
	s_and_saveexec_b64 s[0:1], vcc
	v_lshlrev_b64 v[70:71], 10, v[140:141]
	v_lshl_add_u64 v[70:71], s[10:11], 0, v[70:71]
	v_lshl_add_u64 v[70:71], v[132:133], 1, v[70:71]
	global_store_dwordx4 v[70:71], v[66:69], off sc1
	s_nop 1
.LBB0_1613:
	s_or_b64 exec, exec, s[0:1]
	v_mul_f32_e32 v60, 0x3c800000, v60
	v_mul_f32_e32 v67, 0xbfb8aa3b, v60
	v_exp_f32_e32 v67, v67
	v_mul_f32_e32 v56, 0x3c800000, v56
	v_mul_f32_e32 v57, 0x3c800000, v57
	v_mul_f32_e32 v58, 0x3c800000, v58
	v_add_f32_e32 v67, 1.0, v67
	v_rcp_f32_e32 v67, v67
	v_mul_f32_e32 v59, 0x3c800000, v59
	v_mul_f32_e32 v52, 0x3c800000, v52
	v_mul_f32_e32 v48, 0x3c800000, v48
	v_mul_f32_e32 v60, v60, v67
	v_mul_f32_e32 v56, v60, v56
	v_mul_f32_e32 v60, 0x3c800000, v61
	v_mul_f32_e32 v61, 0xbfb8aa3b, v60
	v_exp_f32_e32 v61, v61
	v_mul_f32_e32 v49, 0x3c800000, v49
	v_add_u32_e32 v66, 0x80, v156
	v_cmp_gt_i32_e32 vcc, s40, v66
	v_add_f32_e32 v61, 1.0, v61
	v_rcp_f32_e32 v61, v61
	s_waitcnt vmcnt(7)
	v_mul_f32_e32 v56, v56, v160
	v_mul_f32_e32 v60, v60, v61
	v_mul_f32_e32 v57, v60, v57
	v_mul_f32_e32 v60, 0x3c800000, v62
	v_mul_f32_e32 v61, 0xbfb8aa3b, v60
	v_exp_f32_e32 v61, v61
	v_mul_f32_e32 v57, v57, v160
	v_add_f32_e32 v61, 1.0, v61
	v_rcp_f32_e32 v61, v61
	s_nop 0
	v_mul_f32_e32 v60, v60, v61
	v_mul_f32_e32 v58, v60, v58
	v_mul_f32_e32 v60, 0x3c800000, v63
	v_mul_f32_e32 v61, 0xbfb8aa3b, v60
	v_exp_f32_e32 v61, v61
	v_mul_f32_e32 v58, v58, v160
	v_add_f32_e32 v61, 1.0, v61
	v_rcp_f32_e32 v61, v61
	s_nop 0
	v_mul_f32_e32 v60, v60, v61
	v_mul_f32_e32 v59, v60, v59
	v_mul_f32_e32 v60, 0xbfb8aa3b, v52
	v_exp_f32_e32 v60, v60
	v_mul_f32_e32 v59, v59, v160
	v_add_f32_e32 v60, 1.0, v60
	v_rcp_f32_e32 v60, v60
	s_nop 0
	v_mul_f32_e32 v52, v52, v60
	v_mul_f32_e32 v48, v52, v48
	v_mul_f32_e32 v52, v48, v160
	v_mul_f32_e32 v48, 0x3c800000, v53
	v_mul_f32_e32 v53, 0xbfb8aa3b, v48
	v_exp_f32_e32 v53, v53
	s_nop 0
	v_add_f32_e32 v53, 1.0, v53
	v_rcp_f32_e32 v53, v53
	s_nop 0
	v_mul_f32_e32 v48, v48, v53
	v_mul_f32_e32 v48, v48, v49
	v_mul_f32_e32 v53, v48, v160
	v_mul_f32_e32 v48, 0x3c800000, v54
	v_mul_f32_e32 v49, 0xbfb8aa3b, v48
	v_exp_f32_e32 v49, v49
	s_nop 0
	v_add_f32_e32 v49, 1.0, v49
	v_rcp_f32_e32 v49, v49
	s_nop 0
	v_mul_f32_e32 v48, v48, v49
	v_mul_f32_e32 v49, 0x3c800000, v50
	v_mul_f32_e32 v48, v48, v49
	v_mul_f32_e32 v54, v48, v160
	v_mul_f32_e32 v48, 0x3c800000, v55
	v_mul_f32_e32 v49, 0xbfb8aa3b, v48
	v_exp_f32_e32 v49, v49
	s_nop 0
	v_add_f32_e32 v49, 1.0, v49
	v_rcp_f32_e32 v49, v49
	s_nop 0
	v_mul_f32_e32 v48, v48, v49
	v_mul_f32_e32 v49, 0x3c800000, v51
	v_mul_f32_e32 v48, v48, v49
	v_mul_f32_e32 v51, v48, v160
	v_cvt_pk_bf16_f32 v48, v56, v57
	v_cvt_pk_bf16_f32 v49, v58, v59
	v_cvt_pk_bf16_f32 v50, v52, v53
	v_cvt_pk_bf16_f32 v51, v54, v51
	s_and_saveexec_b64 s[0:1], vcc
	v_lshlrev_b64 v[52:53], 10, v[138:139]
	v_lshl_add_u64 v[52:53], s[10:11], 0, v[52:53]
	v_lshl_add_u64 v[52:53], v[132:133], 1, v[52:53]
	global_store_dwordx4 v[52:53], v[48:51], off sc1
	s_nop 1
; __device__ __forceinline__ unsigned cvt_pk_bf16(float lo, float hi) { unsigned r; asm volatile("v_cvt_pk_bf16_f32 %0, %1, %2" : "=v"(r) : "v"(lo), "v"(hi)); return r; }
; __device__ __forceinline__ void st_wt16(void* p, u32x4 v) { asm volatile("global_store_dwordx4 %0, %1, off sc1\n\ts_nop 1" :: "v"(p), "v"(v) : "memory"); }
;     __device__ __forceinline__ void operator()(const f32x4 (&acc)[2][2][4][2], const Unit& u, int wr, int wc, int fr, int fq) const {
;     ...
;         for (int ai = 0; ai < 2; ++ai)
; #pragma unroll
;             for (int m = 0; m < 4; ++m) {
;                 const int r = ai * HALF + wr * 64 + m * 16 + fr; const bool valid = r < u.rows;
;                 const int slot = slots[ai * 4 + m];
;                 const float sc = scv[ai * 4 + m], gw = gwv[ai * 4 + m]; float o[8];
; #pragma unroll
;                 for (int n = 0; n < 2; ++n) { const f32x4 g = acc[ai][0][m][n] * sc, up = acc[ai][1][m][n] * sc;
; #pragma unroll
;                     for (int j = 0; j < 4; ++j) o[4 * n + j] = g[j] * __builtin_amdgcn_rcpf(1.0f + __expf(-g[j])) * up[j] * gw; }
;                 u32x4 w; w.x = cvt_pk_bf16(o[0], o[1]); w.y = cvt_pk_bf16(o[2], o[3]); w.z = cvt_pk_bf16(o[4], o[5]); w.w = cvt_pk_bf16(o[6], o[7]);
;                 if (valid) st_wt16(hid + (size_t)slot * 512 + f0, w);
;             }
.LBB0_1615:
	s_or_b64 exec, exec, s[0:1]
	v_mul_f32_e32 v44, 0x3c800000, v44
	v_mul_f32_e32 v48, 0xbfb8aa3b, v44
	v_exp_f32_e32 v48, v48
	v_mul_f32_e32 v40, 0x3c800000, v40
	v_mul_f32_e32 v41, 0x3c800000, v41
	v_mul_f32_e32 v42, 0x3c800000, v42
	v_add_f32_e32 v48, 1.0, v48
	v_rcp_f32_e32 v48, v48
	v_mul_f32_e32 v43, 0x3c800000, v43
	v_mul_f32_e32 v36, 0x3c800000, v36
	v_mul_f32_e32 v32, 0x3c800000, v32
	v_mul_f32_e32 v44, v44, v48
	v_mul_f32_e32 v40, v44, v40
	v_mul_f32_e32 v44, 0x3c800000, v45
	v_mul_f32_e32 v45, 0xbfb8aa3b, v44
	v_exp_f32_e32 v45, v45
	v_mul_f32_e32 v33, 0x3c800000, v33
	s_waitcnt vmcnt(7)
	v_mul_f32_e32 v40, v40, v159
	v_add_f32_e32 v45, 1.0, v45
	v_rcp_f32_e32 v45, v45
	s_nop 0
	v_mul_f32_e32 v44, v44, v45
	v_mul_f32_e32 v41, v44, v41
	v_mul_f32_e32 v44, 0x3c800000, v46
	v_mul_f32_e32 v45, 0xbfb8aa3b, v44
	v_exp_f32_e32 v45, v45
	v_mul_f32_e32 v41, v41, v159
	v_add_f32_e32 v45, 1.0, v45
	v_rcp_f32_e32 v45, v45
	s_nop 0
	v_mul_f32_e32 v44, v44, v45
	v_mul_f32_e32 v42, v44, v42
	v_mul_f32_e32 v44, 0x3c800000, v47
	v_mul_f32_e32 v45, 0xbfb8aa3b, v44
	v_exp_f32_e32 v45, v45
	v_mul_f32_e32 v42, v42, v159
	v_add_f32_e32 v45, 1.0, v45
	v_rcp_f32_e32 v45, v45
	s_nop 0
	v_mul_f32_e32 v44, v44, v45
	v_mul_f32_e32 v43, v44, v43
	v_mul_f32_e32 v44, 0xbfb8aa3b, v36
	v_exp_f32_e32 v44, v44
	v_mul_f32_e32 v43, v43, v159
	v_add_f32_e32 v44, 1.0, v44
	v_rcp_f32_e32 v44, v44
	s_nop 0
	v_mul_f32_e32 v36, v36, v44
	v_mul_f32_e32 v32, v36, v32
	v_mul_f32_e32 v36, v32, v159
	v_mul_f32_e32 v32, 0x3c800000, v37
	v_mul_f32_e32 v37, 0xbfb8aa3b, v32
	v_exp_f32_e32 v37, v37
	s_nop 0
	v_add_f32_e32 v37, 1.0, v37
	v_rcp_f32_e32 v37, v37
	s_nop 0
	v_mul_f32_e32 v32, v32, v37
	v_mul_f32_e32 v32, v32, v33
	v_mul_f32_e32 v37, v32, v159
	v_mul_f32_e32 v32, 0x3c800000, v38
	v_mul_f32_e32 v33, 0xbfb8aa3b, v32
	v_exp_f32_e32 v33, v33
	s_nop 0
	v_add_f32_e32 v33, 1.0, v33
	v_rcp_f32_e32 v33, v33
	s_nop 0
	v_mul_f32_e32 v32, v32, v33
	v_mul_f32_e32 v33, 0x3c800000, v34
	v_mul_f32_e32 v32, v32, v33
	v_mul_f32_e32 v38, v32, v159
	v_mul_f32_e32 v32, 0x3c800000, v39
	v_mul_f32_e32 v33, 0xbfb8aa3b, v32
	v_exp_f32_e32 v33, v33
	s_nop 0
	v_add_f32_e32 v33, 1.0, v33
	v_rcp_f32_e32 v33, v33
	s_nop 0
	v_mul_f32_e32 v32, v32, v33
	v_mul_f32_e32 v33, 0x3c800000, v35
	v_mul_f32_e32 v32, v32, v33
	v_mul_f32_e32 v35, v32, v159
	v_add_u32_e32 v32, 0x90, v156
	v_cmp_gt_i32_e32 vcc, s40, v32
	v_cvt_pk_bf16_f32 v32, v40, v41
	v_cvt_pk_bf16_f32 v33, v42, v43
	v_cvt_pk_bf16_f32 v34, v36, v37
	v_cvt_pk_bf16_f32 v35, v38, v35
	s_and_saveexec_b64 s[0:1], vcc
	v_lshlrev_b64 v[36:37], 10, v[136:137]
	v_lshl_add_u64 v[36:37], s[10:11], 0, v[36:37]
	v_lshl_add_u64 v[36:37], v[132:133], 1, v[36:37]
	global_store_dwordx4 v[36:37], v[32:35], off sc1
	s_nop 1
; __device__ __forceinline__ unsigned cvt_pk_bf16(float lo, float hi) { unsigned r; asm volatile("v_cvt_pk_bf16_f32 %0, %1, %2" : "=v"(r) : "v"(lo), "v"(hi)); return r; }
; __device__ __forceinline__ void st_wt16(void* p, u32x4 v) { asm volatile("global_store_dwordx4 %0, %1, off sc1\n\ts_nop 1" :: "v"(p), "v"(v) : "memory"); }
;     __device__ __forceinline__ void operator()(const f32x4 (&acc)[2][2][4][2], const Unit& u, int wr, int wc, int fr, int fq) const {
;     ...
;         for (int ai = 0; ai < 2; ++ai)
; #pragma unroll
;             for (int m = 0; m < 4; ++m) {
;                 const int r = ai * HALF + wr * 64 + m * 16 + fr; const bool valid = r < u.rows;
;                 const int slot = slots[ai * 4 + m];
;                 const float sc = scv[ai * 4 + m], gw = gwv[ai * 4 + m]; float o[8];
; #pragma unroll
;                 for (int n = 0; n < 2; ++n) { const f32x4 g = acc[ai][0][m][n] * sc, up = acc[ai][1][m][n] * sc;
; #pragma unroll
;                     for (int j = 0; j < 4; ++j) o[4 * n + j] = g[j] * __builtin_amdgcn_rcpf(1.0f + __expf(-g[j])) * up[j] * gw; }
;                 u32x4 w; w.x = cvt_pk_bf16(o[0], o[1]); w.y = cvt_pk_bf16(o[2], o[3]); w.z = cvt_pk_bf16(o[4], o[5]); w.w = cvt_pk_bf16(o[6], o[7]);
;                 if (valid) st_wt16(hid + (size_t)slot * 512 + f0, w);
;             }
.LBB0_1617:
	s_or_b64 exec, exec, s[0:1]
	v_mul_f32_e32 v24, 0x3c800000, v24
	v_mul_f32_e32 v32, 0xbfb8aa3b, v24
	v_exp_f32_e32 v32, v32
	v_mul_f32_e32 v28, 0x3c800000, v28
	v_mul_f32_e32 v25, 0x3c800000, v25
	v_mul_f32_e32 v26, 0x3c800000, v26
	v_add_f32_e32 v32, 1.0, v32
	v_rcp_f32_e32 v32, v32
	v_mul_f32_e32 v27, 0x3c800000, v27
	v_mul_f32_e32 v16, 0x3c800000, v16
	v_mul_f32_e32 v20, 0x3c800000, v20
	v_mul_f32_e32 v24, v24, v32
	v_mul_f32_e32 v24, v24, v28
	v_mul_f32_e32 v28, 0xbfb8aa3b, v25
	v_exp_f32_e32 v28, v28
	s_waitcnt vmcnt(7)
	v_mul_f32_e32 v24, v24, v158
	v_add_f32_e32 v28, 1.0, v28
	v_rcp_f32_e32 v28, v28
	s_nop 0
	v_mul_f32_e32 v25, v25, v28
	v_mul_f32_e32 v28, 0x3c800000, v29
	v_mul_f32_e32 v25, v25, v28
	v_mul_f32_e32 v28, 0xbfb8aa3b, v26
	v_exp_f32_e32 v28, v28
	v_mul_f32_e32 v25, v25, v158
	v_add_f32_e32 v28, 1.0, v28
	v_rcp_f32_e32 v28, v28
	s_nop 0
	v_mul_f32_e32 v26, v26, v28
	v_mul_f32_e32 v28, 0x3c800000, v30
	v_mul_f32_e32 v26, v26, v28
	v_mul_f32_e32 v28, 0xbfb8aa3b, v27
	v_exp_f32_e32 v28, v28
	v_mul_f32_e32 v26, v26, v158
	v_add_f32_e32 v28, 1.0, v28
	v_rcp_f32_e32 v28, v28
	s_nop 0
	v_mul_f32_e32 v27, v27, v28
	v_mul_f32_e32 v28, 0x3c800000, v31
	v_mul_f32_e32 v27, v27, v28
	v_mul_f32_e32 v28, 0xbfb8aa3b, v16
	v_exp_f32_e32 v28, v28
	v_mul_f32_e32 v27, v27, v158
	v_add_f32_e32 v28, 1.0, v28
	v_rcp_f32_e32 v28, v28
	s_nop 0
	v_mul_f32_e32 v16, v16, v28
	v_mul_f32_e32 v16, v16, v20
	v_mul_f32_e32 v20, v16, v158
	v_mul_f32_e32 v16, 0x3c800000, v17
	v_mul_f32_e32 v17, 0xbfb8aa3b, v16
	v_exp_f32_e32 v17, v17
	s_nop 0
	v_add_f32_e32 v17, 1.0, v17
	v_rcp_f32_e32 v17, v17
	s_nop 0
	v_mul_f32_e32 v16, v16, v17
	v_mul_f32_e32 v17, 0x3c800000, v21
	v_mul_f32_e32 v16, v16, v17
	v_mul_f32_e32 v21, v16, v158
	v_mul_f32_e32 v16, 0x3c800000, v18
	v_mul_f32_e32 v17, 0xbfb8aa3b, v16
	v_exp_f32_e32 v17, v17
	s_nop 0
	v_add_f32_e32 v17, 1.0, v17
	v_rcp_f32_e32 v17, v17
	s_nop 0
	v_mul_f32_e32 v16, v16, v17
	v_mul_f32_e32 v17, 0x3c800000, v22
	v_mul_f32_e32 v16, v16, v17
	v_mul_f32_e32 v22, v16, v158
	v_mul_f32_e32 v16, 0x3c800000, v19
	v_mul_f32_e32 v17, 0xbfb8aa3b, v16
	v_exp_f32_e32 v17, v17
	s_nop 0
	v_add_f32_e32 v17, 1.0, v17
	v_rcp_f32_e32 v17, v17
	s_nop 0
	v_mul_f32_e32 v16, v16, v17
	v_mul_f32_e32 v17, 0x3c800000, v23
	v_mul_f32_e32 v16, v16, v17
	v_mul_f32_e32 v19, v16, v158
	v_add_u32_e32 v16, 0xa0, v156
	v_cmp_gt_i32_e32 vcc, s40, v16
	v_cvt_pk_bf16_f32 v16, v24, v25
	v_cvt_pk_bf16_f32 v17, v26, v27
	v_cvt_pk_bf16_f32 v18, v20, v21
	v_cvt_pk_bf16_f32 v19, v22, v19
	s_and_saveexec_b64 s[0:1], vcc
	v_lshlrev_b64 v[20:21], 10, v[134:135]
	v_lshl_add_u64 v[20:21], s[10:11], 0, v[20:21]
	v_lshl_add_u64 v[20:21], v[132:133], 1, v[20:21]
	global_store_dwordx4 v[20:21], v[16:19], off sc1
	s_nop 1
.LBB0_1619:
	s_or_b64 exec, exec, s[0:1]
	v_mul_f32_e32 v8, 0x3c800000, v8
	v_mul_f32_e32 v16, 0xbfb8aa3b, v8
	v_exp_f32_e32 v16, v16
	v_mul_f32_e32 v12, 0x3c800000, v0
	v_mul_f32_e32 v9, 0x3c800000, v9
	v_mul_f32_e32 v10, 0x3c800000, v10
	v_add_f32_e32 v16, 1.0, v16
	v_rcp_f32_e32 v16, v16
	v_mul_f32_e32 v11, 0x3c800000, v11
	v_mul_f32_e32 v0, 0x3c800000, v230
	v_mul_f32_e32 v4, 0x3c800000, v4
	v_mul_f32_e32 v8, v8, v16
	v_mul_f32_e32 v8, v8, v12
	v_mul_f32_e32 v12, 0xbfb8aa3b, v9
	v_exp_f32_e32 v12, v12
	s_waitcnt vmcnt(7)
	v_mul_f32_e32 v8, v8, v157
	v_add_f32_e32 v12, 1.0, v12
	v_rcp_f32_e32 v12, v12
	s_nop 0
	v_mul_f32_e32 v9, v9, v12
	v_mul_f32_e32 v12, 0x3c800000, v1
	v_mul_f32_e32 v9, v9, v12
	v_mul_f32_e32 v12, 0xbfb8aa3b, v10
	v_exp_f32_e32 v12, v12
	v_mul_f32_e32 v9, v9, v157
	v_add_f32_e32 v12, 1.0, v12
	v_rcp_f32_e32 v12, v12
	s_nop 0
	v_mul_f32_e32 v10, v10, v12
	v_mul_f32_e32 v12, 0x3c800000, v2
	v_mul_f32_e32 v10, v10, v12
	v_mul_f32_e32 v12, 0xbfb8aa3b, v11
	v_exp_f32_e32 v12, v12
	v_mul_f32_e32 v10, v10, v157
	v_add_f32_e32 v12, 1.0, v12
	v_rcp_f32_e32 v12, v12
	s_nop 0
	v_mul_f32_e32 v11, v11, v12
	v_mul_f32_e32 v12, 0x3c800000, v3
	v_mul_f32_e32 v11, v11, v12
	v_mul_f32_e32 v12, 0xbfb8aa3b, v0
	v_exp_f32_e32 v12, v12
	v_mul_f32_e32 v11, v11, v157
	v_add_f32_e32 v12, 1.0, v12
	v_rcp_f32_e32 v12, v12
	s_nop 0
	v_mul_f32_e32 v0, v0, v12
	v_mul_f32_e32 v0, v0, v4
	v_mul_f32_e32 v4, v0, v157
	v_mul_f32_e32 v0, 0x3c800000, v231
	v_mul_f32_e32 v1, 0xbfb8aa3b, v0
	v_exp_f32_e32 v1, v1
	s_nop 0
	v_add_f32_e32 v1, 1.0, v1
	v_rcp_f32_e32 v1, v1
	s_nop 0
	v_mul_f32_e32 v0, v0, v1
	v_mul_f32_e32 v1, 0x3c800000, v5
	v_mul_f32_e32 v0, v0, v1
	v_mul_f32_e32 v5, v0, v157
	v_mul_f32_e32 v0, 0x3c800000, v232
	v_mul_f32_e32 v1, 0xbfb8aa3b, v0
	v_exp_f32_e32 v1, v1
	s_nop 0
	v_add_f32_e32 v1, 1.0, v1
	v_rcp_f32_e32 v1, v1
	s_nop 0
	v_mul_f32_e32 v0, v0, v1
	v_mul_f32_e32 v1, 0x3c800000, v6
	v_mul_f32_e32 v0, v0, v1
	v_mul_f32_e32 v6, v0, v157
	v_mul_f32_e32 v0, 0x3c800000, v233
	v_mul_f32_e32 v1, 0xbfb8aa3b, v0
	v_exp_f32_e32 v1, v1
	s_nop 0
	v_add_f32_e32 v1, 1.0, v1
	v_rcp_f32_e32 v1, v1
	s_nop 0
	v_mul_f32_e32 v0, v0, v1
	v_mul_f32_e32 v1, 0x3c800000, v7
	v_mul_f32_e32 v0, v0, v1
	v_mul_f32_e32 v3, v0, v157
	v_add_u32_e32 v0, 0xb0, v156
	v_cmp_gt_i32_e32 vcc, s40, v0
	v_cvt_pk_bf16_f32 v0, v8, v9
	v_cvt_pk_bf16_f32 v1, v10, v11
	v_cvt_pk_bf16_f32 v2, v4, v5
	v_cvt_pk_bf16_f32 v3, v6, v3
	s_and_saveexec_b64 s[0:1], vcc
	s_cbranch_execz .LBB0_1621
	v_lshlrev_b64 v[4:5], 10, v[130:131]
	v_lshl_add_u64 v[4:5], s[10:11], 0, v[4:5]
	v_lshl_add_u64 v[4:5], v[132:133], 1, v[4:5]
	global_store_dwordx4 v[4:5], v[0:3], off sc1
	s_nop 1
